# norm1 / final combine: the 32 loads of the per-slot expert outputs no longer carry the nt hint (checking whether default caching of the read-once rows matters); plus previous changes
# speedup vs baseline: 1.0076x; 1.0009x over previous
; __device__ __forceinline__ float bf_lo(unsigned w) { return __uint_as_float(w << 16); }
; __device__ __forceinline__ float bf_hi(unsigned w) { return __uint_as_float(w & 0xffff0000u); }
;     __device__ __forceinline__ float* mods() const { return (float*)(ws + WS_MODS); }
;     __device__ __forceinline__ bf16_t* Y() const { return (bf16_t*)(ws + WS_Y); }
; __device__ __forceinline__ void phase_norm1(const Frame& F, const Params& P, int l, const float* xs, long long dctx, bool combine, float* xw, long long dctxw) {
;     ...
;         const float* xr = xrow_ptr(xs, dctx, row);
;         const int b = row < TL ? (row >> 13) : 8;
;         const float* md = F.mods() + (size_t)(l * 9 + b) * 6144;
;         f32x4 v[4]; float ss = 0.f;
; #pragma unroll
;         for (int j = 0; j < 4; ++j) v[j] = *(const f32x4*)(xr + F.lane * 4 + 256 * j);
;         if (combine) {
;             const float* g5 = F.mods() + (size_t)((l - 1) * 9 + b) * 6144 + 5 * 1024;
;             const bf16_t* yr = F.Y() + (size_t)row * 4 * DM;
;             float* xo = xw + (size_t)row * DM + (row >= TL ? dctxw : 0ll);
; #pragma unroll
;             for (int j = 0; j < 4; ++j) {
;                 const int col = F.lane * 4 + 256 * j;
;                 f32x4 s = (f32x4){0.f, 0.f, 0.f, 0.f};
; #pragma unroll
;                 for (int k = 0; k < 4; ++k) { const u32x2 w = __builtin_nontemporal_load((const u32x2*)(yr + (size_t)k * DM + col));     s[0] += bf_lo(w.x); s[1] += bf_hi(w.x); s[2] += bf_lo(w.y); s[3] += bf_hi(w.y); }
;                 v[j] += *(const f32x4*)(g5 + col) * s;
;                 *(f32x4*)(xo + col) = v[j];
;             }
;         }
.LBB0_171:
	s_cmp_gt_i32 s44, 0xffff
	s_cselect_b64 s[8:9], -1, 0
	s_and_b64 s[18:19], s[8:9], exec
	s_cselect_b32 s19, s43, 0
	s_cselect_b32 s18, s42, 0
	v_lshl_add_u64 v[2:3], s[52:53], 0, v[20:21]
	v_lshl_add_u64 v[2:3], s[18:19], 2, v[2:3]
	global_load_dwordx4 v[14:17], v[2:3], off
	global_load_dwordx4 v[10:13], v[2:3], off offset:1024
	global_load_dwordx4 v[6:9], v[2:3], off offset:2048
	s_nop 0
	global_load_dwordx4 v[2:5], v[2:3], off offset:3072
	s_min_i32 s2, s44, 0x10000
	s_andn2_b64 vcc, exec, s[40:41]
	s_ashr_i32 s2, s2, 13
	s_cbranch_vccnz .LBB0_170
	s_mul_i32 s18, s2, 0x6000
	s_mul_hi_i32 s7, s2, 0x6000
	s_add_u32 s18, s0, s18
	s_addc_u32 s7, s1, s7
	s_add_u32 s28, s18, 0x5000
	s_addc_u32 s29, s7, 0
	v_lshl_add_u64 v[22:23], s[46:47], 0, v[146:147]
	s_mov_b32 s7, 0x1c316000
	v_add_co_u32_e32 v24, vcc, s7, v22
	s_mov_b32 s7, 0x1c317000
	s_nop 0
	v_addc_co_u32_e32 v25, vcc, 0, v23, vcc
	global_load_dwordx2 v[32:33], v[24:25], off offset:256
	global_load_dwordx2 v[34:35], v[24:25], off offset:2304
	v_add_co_u32_e32 v26, vcc, s7, v22
	s_and_b64 s[8:9], s[8:9], exec
	s_nop 0
	v_addc_co_u32_e32 v27, vcc, 0, v23, vcc
	global_load_dwordx2 v[22:23], v[26:27], off offset:256
	global_load_dwordx2 v[36:37], v[26:27], off offset:2304
	global_load_dwordx4 v[80:83], v30, s[28:29]
	global_load_dwordx2 v[84:85], v[24:25], off offset:768
	global_load_dwordx2 v[86:87], v[24:25], off offset:2816
	global_load_dwordx2 v[88:89], v[26:27], off offset:768
	global_load_dwordx2 v[90:91], v[26:27], off offset:2816
	global_load_dwordx4 v[92:95], v1, s[28:29]
	global_load_dwordx2 v[96:97], v[24:25], off offset:1280
	global_load_dwordx2 v[98:99], v[24:25], off offset:3328
	global_load_dwordx2 v[100:101], v[26:27], off offset:1280
	global_load_dwordx2 v[102:103], v[26:27], off offset:3328
	global_load_dwordx4 v[104:107], v28, s[28:29]
	global_load_dwordx2 v[108:109], v[24:25], off offset:1792
	global_load_dwordx2 v[110:111], v[24:25], off offset:3840
	global_load_dwordx2 v[112:113], v[26:27], off offset:1792
	global_load_dwordx2 v[114:115], v[26:27], off offset:3840
	global_load_dwordx4 v[116:119], v29, s[28:29]
	s_cselect_b32 s9, s61, 0
	s_cselect_b32 s8, s60, 0
	s_waitcnt vmcnt(15)
	v_lshlrev_b32_e32 v38, 16, v32
	v_and_b32_e32 v39, 0xffff0000, v32
	v_lshlrev_b32_e32 v32, 16, v33
	v_and_b32_e32 v33, 0xffff0000, v33
	v_pk_add_f32 v[38:39], v[38:39], 0 op_sel_hi:[1,0]
	v_lshlrev_b32_e32 v40, 16, v34
	v_and_b32_e32 v41, 0xffff0000, v34
	v_pk_add_f32 v[32:33], v[32:33], 0 op_sel_hi:[1,0]
	v_lshlrev_b32_e32 v34, 16, v35
	v_and_b32_e32 v35, 0xffff0000, v35
	v_pk_add_f32 v[38:39], v[38:39], v[40:41]
	v_lshlrev_b32_e32 v40, 16, v22
	v_and_b32_e32 v41, 0xffff0000, v22
	v_pk_add_f32 v[32:33], v[32:33], v[34:35]
	v_lshlrev_b32_e32 v22, 16, v23
	v_and_b32_e32 v23, 0xffff0000, v23
	v_pk_add_f32 v[22:23], v[32:33], v[22:23]
	v_lshlrev_b32_e32 v32, 16, v37
	v_and_b32_e32 v33, 0xffff0000, v37
	v_pk_add_f32 v[22:23], v[22:23], v[32:33]
	v_pk_add_f32 v[38:39], v[38:39], v[40:41]
	v_lshlrev_b32_e32 v40, 16, v36
	v_and_b32_e32 v41, 0xffff0000, v36
	v_pk_add_f32 v[38:39], v[38:39], v[40:41]
	v_pk_fma_f32 v[16:17], v[82:83], v[22:23], v[16:17]
	v_lshl_add_u64 v[22:23], s[50:51], 0, v[20:21]
	v_pk_fma_f32 v[14:15], v[80:81], v[38:39], v[14:15]
	v_lshl_add_u64 v[22:23], s[8:9], 2, v[22:23]
	global_store_dwordx4 v[22:23], v[14:17], off
	s_waitcnt vmcnt(11)
	v_lshlrev_b32_e32 v40, 16, v84
	v_and_b32_e32 v41, 0xffff0000, v84
	v_lshlrev_b32_e32 v32, 16, v85
	v_and_b32_e32 v33, 0xffff0000, v85
	v_lshlrev_b32_e32 v42, 16, v86
	v_and_b32_e32 v43, 0xffff0000, v86
	v_pk_add_f32 v[32:33], v[32:33], 0 op_sel_hi:[1,0]
	v_lshlrev_b32_e32 v34, 16, v87
	v_and_b32_e32 v35, 0xffff0000, v87
	v_pk_add_f32 v[32:33], v[32:33], v[34:35]
	v_lshlrev_b32_e32 v34, 16, v89
	v_and_b32_e32 v35, 0xffff0000, v89
	v_pk_add_f32 v[40:41], v[40:41], 0 op_sel_hi:[1,0]
	v_pk_add_f32 v[32:33], v[32:33], v[34:35]
	v_lshlrev_b32_e32 v34, 16, v91
	v_and_b32_e32 v35, 0xffff0000, v91
	v_pk_add_f32 v[40:41], v[40:41], v[42:43]
	v_lshlrev_b32_e32 v42, 16, v88
	v_and_b32_e32 v43, 0xffff0000, v88
	v_pk_add_f32 v[36:37], v[32:33], v[34:35]
	v_pk_add_f32 v[40:41], v[40:41], v[42:43]
	v_lshlrev_b32_e32 v42, 16, v90
	v_and_b32_e32 v43, 0xffff0000, v90
	v_pk_add_f32 v[40:41], v[40:41], v[42:43]
	v_pk_fma_f32 v[12:13], v[94:95], v[36:37], v[12:13]
	v_pk_fma_f32 v[10:11], v[92:93], v[40:41], v[10:11]
	global_store_dwordx4 v[22:23], v[10:13], off offset:1024
	s_waitcnt vmcnt(7)
	v_lshlrev_b32_e32 v40, 16, v96
	v_and_b32_e32 v41, 0xffff0000, v96
	v_lshlrev_b32_e32 v32, 16, v97
	v_and_b32_e32 v33, 0xffff0000, v97
	v_lshlrev_b32_e32 v42, 16, v98
	v_and_b32_e32 v43, 0xffff0000, v98
	v_pk_add_f32 v[32:33], v[32:33], 0 op_sel_hi:[1,0]
	v_lshlrev_b32_e32 v34, 16, v99
	v_and_b32_e32 v35, 0xffff0000, v99
	v_pk_add_f32 v[32:33], v[32:33], v[34:35]
	v_lshlrev_b32_e32 v34, 16, v101
	v_and_b32_e32 v35, 0xffff0000, v101
	v_pk_add_f32 v[40:41], v[40:41], 0 op_sel_hi:[1,0]
	v_pk_add_f32 v[32:33], v[32:33], v[34:35]
	v_lshlrev_b32_e32 v34, 16, v103
	v_and_b32_e32 v35, 0xffff0000, v103
	v_pk_add_f32 v[40:41], v[40:41], v[42:43]
	v_lshlrev_b32_e32 v42, 16, v100
	v_and_b32_e32 v43, 0xffff0000, v100
	v_pk_add_f32 v[36:37], v[32:33], v[34:35]
	v_pk_add_f32 v[40:41], v[40:41], v[42:43]
	v_lshlrev_b32_e32 v42, 16, v102
	v_and_b32_e32 v43, 0xffff0000, v102
	v_pk_add_f32 v[40:41], v[40:41], v[42:43]
	v_pk_fma_f32 v[8:9], v[106:107], v[36:37], v[8:9]
	v_pk_fma_f32 v[6:7], v[104:105], v[40:41], v[6:7]
	global_store_dwordx4 v[22:23], v[6:9], off offset:2048
	s_nop 0
	s_nop 0
	s_nop 0
	s_waitcnt vmcnt(3)
	v_lshlrev_b32_e32 v36, 16, v108
	v_and_b32_e32 v37, 0xffff0000, v108
	v_lshlrev_b32_e32 v32, 16, v109
	v_and_b32_e32 v33, 0xffff0000, v109
	v_pk_add_f32 v[36:37], v[36:37], 0 op_sel_hi:[1,0]
	v_lshlrev_b32_e32 v38, 16, v110
	v_and_b32_e32 v39, 0xffff0000, v110
	v_pk_add_f32 v[32:33], v[32:33], 0 op_sel_hi:[1,0]
	v_lshlrev_b32_e32 v24, 16, v111
	v_and_b32_e32 v25, 0xffff0000, v111
	v_pk_add_f32 v[36:37], v[36:37], v[38:39]
	v_lshlrev_b32_e32 v38, 16, v112
	v_and_b32_e32 v39, 0xffff0000, v112
	v_pk_add_f32 v[24:25], v[32:33], v[24:25]
	v_lshlrev_b32_e32 v32, 16, v113
	v_and_b32_e32 v33, 0xffff0000, v113
	v_pk_add_f32 v[36:37], v[36:37], v[38:39]
	v_lshlrev_b32_e32 v38, 16, v114
	v_and_b32_e32 v39, 0xffff0000, v114
	v_pk_add_f32 v[24:25], v[24:25], v[32:33]
	v_lshlrev_b32_e32 v26, 16, v115
	v_and_b32_e32 v27, 0xffff0000, v115
	v_pk_add_f32 v[32:33], v[24:25], v[26:27]
	v_pk_add_f32 v[36:37], v[36:37], v[38:39]
	v_pk_fma_f32 v[4:5], v[118:119], v[32:33], v[4:5]
	v_pk_fma_f32 v[2:3], v[116:117], v[36:37], v[2:3]
	global_store_dwordx4 v[22:23], v[2:5], off offset:3072
	s_branch .LBB0_170

; __device__ __forceinline__ float bf_lo(unsigned w) { return __uint_as_float(w << 16); }
; __device__ __forceinline__ float bf_hi(unsigned w) { return __uint_as_float(w & 0xffff0000u); }
;     __device__ __forceinline__ float* mods() const { return (float*)(ws + WS_MODS); }
;     __device__ __forceinline__ bf16_t* Y() const { return (bf16_t*)(ws + WS_Y); }
; __device__ __forceinline__ void phase_final(const Frame& F, const Params& P) {
;     ...
;         float* xr = P.out + (size_t)row * DM;
;         const float* g5 = F.mods() + (size_t)((NLAYER - 1) * 9 + (row >> 13)) * 6144 + 5 * 1024;
;         const bf16_t* yr = F.Y() + (size_t)row * 4 * DM;
;         f32x4 v[4]; float ss = 0.f;
; #pragma unroll
;         for (int j = 0; j < 4; ++j) {
;             const int col = F.lane * 4 + 256 * j;
;             v[j] = *(const f32x4*)(xr + col);
;             f32x4 s = (f32x4){0.f, 0.f, 0.f, 0.f};
; #pragma unroll
;             for (int k = 0; k < 4; ++k) { const u32x2 w = __builtin_nontemporal_load((const u32x2*)(yr + (size_t)k * DM + col));     s[0] += bf_lo(w.x); s[1] += bf_hi(w.x); s[2] += bf_lo(w.y); s[3] += bf_hi(w.y); }
;             v[j] += *(const f32x4*)(g5 + col) * s;
.LBB0_1932:
	s_ashr_i32 s3, s0, 13
	v_add_co_u32_e32 v36, vcc, s1, v0
	s_add_i32 s3, s3, 9
	global_load_dwordx2 v[8:9], v[0:1], off
	global_load_dwordx2 v[6:7], v[0:1], off offset:2048
	global_load_dwordx2 v[52:53], v[0:1], off offset:512
	global_load_dwordx2 v[54:55], v[0:1], off offset:2560
	global_load_dwordx2 v[56:57], v[0:1], off offset:1024
	global_load_dwordx2 v[58:59], v[0:1], off offset:3072
	global_load_dwordx2 v[60:61], v[0:1], off offset:1536
	global_load_dwordx2 v[62:63], v[0:1], off offset:3584
	v_addc_co_u32_e32 v37, vcc, 0, v1, vcc
	s_mul_hi_i32 s4, s3, 0x6000
	s_mulk_i32 s3, 0x6000
	global_load_dwordx4 v[16:19], v[4:5], off offset:-3072
	global_load_dwordx4 v[20:23], v[4:5], off offset:-2048
	global_load_dwordx4 v[24:27], v[4:5], off offset:-1024
	global_load_dwordx4 v[28:31], v[4:5], off
	global_load_dwordx2 v[64:65], v[36:37], off
	global_load_dwordx2 v[66:67], v[36:37], off offset:2048
	global_load_dwordx2 v[68:69], v[36:37], off offset:512
	global_load_dwordx2 v[70:71], v[36:37], off offset:2560
	global_load_dwordx2 v[72:73], v[36:37], off offset:1024
	global_load_dwordx2 v[74:75], v[36:37], off offset:3072
	global_load_dwordx2 v[76:77], v[36:37], off offset:1536
	global_load_dwordx2 v[78:79], v[36:37], off offset:3584
	s_add_u32 s3, s54, s3
	s_addc_u32 s5, s55, s4
	s_add_u32 s4, s3, 0x45000
	s_addc_u32 s5, s5, 0
	global_load_dwordx4 v[36:39], v10, s[4:5]
	global_load_dwordx4 v[40:43], v11, s[4:5]
	global_load_dwordx4 v[44:47], v12, s[4:5]
	global_load_dwordx4 v[48:51], v13, s[4:5]
	s_add_i32 s0, s0, s6
	v_lshl_add_u64 v[0:1], v[0:1], 0, s[8:9]
	s_cmp_lt_i32 s0, 0x10000
	s_waitcnt vmcnt(23)
	v_lshlrev_b32_e32 v80, 16, v8
	v_and_b32_e32 v81, 0xffff0000, v8
	v_lshlrev_b32_e32 v8, 16, v9
	v_and_b32_e32 v9, 0xffff0000, v9
	s_waitcnt vmcnt(21)
	v_lshlrev_b32_e32 v84, 16, v52
	v_and_b32_e32 v85, 0xffff0000, v52
	v_lshlrev_b32_e32 v82, 16, v6
	v_and_b32_e32 v83, 0xffff0000, v6
	v_lshlrev_b32_e32 v6, 16, v7
	v_and_b32_e32 v7, 0xffff0000, v7
	s_waitcnt vmcnt(20)
	v_lshlrev_b32_e32 v86, 16, v54
	v_and_b32_e32 v87, 0xffff0000, v54
	v_lshlrev_b32_e32 v52, 16, v53
	v_and_b32_e32 v53, 0xffff0000, v53
	s_waitcnt vmcnt(19)
	v_lshlrev_b32_e32 v88, 16, v56
	v_and_b32_e32 v89, 0xffff0000, v56
	v_lshlrev_b32_e32 v56, 16, v57
	v_and_b32_e32 v57, 0xffff0000, v57
	s_waitcnt vmcnt(17)
	v_lshlrev_b32_e32 v92, 16, v60
	v_and_b32_e32 v93, 0xffff0000, v60
	v_lshlrev_b32_e32 v60, 16, v61
	v_and_b32_e32 v61, 0xffff0000, v61
	v_pk_add_f32 v[80:81], v[80:81], 0 op_sel_hi:[1,0]
	v_pk_add_f32 v[8:9], v[8:9], 0 op_sel_hi:[1,0]
	v_pk_add_f32 v[84:85], v[84:85], 0 op_sel_hi:[1,0]
	v_lshlrev_b32_e32 v54, 16, v55
	v_and_b32_e32 v55, 0xffff0000, v55
	v_lshlrev_b32_e32 v90, 16, v58
	v_and_b32_e32 v91, 0xffff0000, v58
	v_lshlrev_b32_e32 v58, 16, v59
	v_and_b32_e32 v59, 0xffff0000, v59
	s_waitcnt vmcnt(16)
	v_lshlrev_b32_e32 v94, 16, v62
	v_and_b32_e32 v95, 0xffff0000, v62
	v_lshlrev_b32_e32 v62, 16, v63
	v_and_b32_e32 v63, 0xffff0000, v63
	v_pk_add_f32 v[52:53], v[52:53], 0 op_sel_hi:[1,0]
	v_pk_add_f32 v[88:89], v[88:89], 0 op_sel_hi:[1,0]
	v_pk_add_f32 v[56:57], v[56:57], 0 op_sel_hi:[1,0]
	v_pk_add_f32 v[92:93], v[92:93], 0 op_sel_hi:[1,0]
	v_pk_add_f32 v[60:61], v[60:61], 0 op_sel_hi:[1,0]
	v_pk_add_f32 v[80:81], v[80:81], v[82:83]
	s_waitcnt vmcnt(11)
	v_lshlrev_b32_e32 v82, 16, v64
	v_and_b32_e32 v83, 0xffff0000, v64
	s_waitcnt vmcnt(10)
	v_lshlrev_b32_e32 v96, 16, v66
	v_and_b32_e32 v97, 0xffff0000, v66
	v_pk_add_f32 v[6:7], v[8:9], v[6:7]
	v_lshlrev_b32_e32 v8, 16, v65
	v_and_b32_e32 v9, 0xffff0000, v65
	v_lshlrev_b32_e32 v64, 16, v67
	v_and_b32_e32 v65, 0xffff0000, v67
	v_pk_add_f32 v[66:67], v[84:85], v[86:87]
	s_waitcnt vmcnt(9)
	v_lshlrev_b32_e32 v84, 16, v68
	v_and_b32_e32 v85, 0xffff0000, v68
	s_waitcnt vmcnt(8)
	v_lshlrev_b32_e32 v86, 16, v70
	v_and_b32_e32 v87, 0xffff0000, v70
	v_pk_add_f32 v[52:53], v[52:53], v[54:55]
	v_lshlrev_b32_e32 v54, 16, v69
	v_and_b32_e32 v55, 0xffff0000, v69
	v_lshlrev_b32_e32 v68, 16, v71
	v_and_b32_e32 v69, 0xffff0000, v71
	v_pk_add_f32 v[70:71], v[88:89], v[90:91]
	s_waitcnt vmcnt(7)
	v_lshlrev_b32_e32 v88, 16, v72
	v_and_b32_e32 v89, 0xffff0000, v72
	s_waitcnt vmcnt(6)
; __device__ __forceinline__ void phase_final(const Frame& F, const Params& P) {
;     ...
;             v[j] += *(const f32x4*)(g5 + col) * s;
;             ss += v[j][0] * v[j][0] + v[j][1] * v[j][1] + v[j][2] * v[j][2] + v[j][3] * v[j][3];
;         }
;         ss = wave_sum(ss);
;         const float rstd = rsqrtf(ss * (1.f / 1024.f) + EPS);
; #pragma unroll
;         for (int j = 0; j < 4; ++j) {
;             const int col = F.lane * 4 + 256 * j;
;             const f32x4 gg = *(const f32x4*)(P.g_final + col);
;             f32x4 o;
; #pragma unroll
;             for (int i = 0; i < 4; ++i) o[i] = v[j][i] * rstd * gg[i];
;             *(f32x4*)(xr + col) = o;
;         }
	v_lshlrev_b32_e32 v90, 16, v74
	v_and_b32_e32 v91, 0xffff0000, v74
	v_pk_add_f32 v[56:57], v[56:57], v[58:59]
	v_lshlrev_b32_e32 v58, 16, v73
	v_and_b32_e32 v59, 0xffff0000, v73
	v_lshlrev_b32_e32 v72, 16, v75
	v_and_b32_e32 v73, 0xffff0000, v75
	v_pk_add_f32 v[74:75], v[92:93], v[94:95]
	s_waitcnt vmcnt(5)
	v_lshlrev_b32_e32 v92, 16, v76
	v_and_b32_e32 v93, 0xffff0000, v76
	s_waitcnt vmcnt(4)
	v_lshlrev_b32_e32 v94, 16, v78
	v_and_b32_e32 v95, 0xffff0000, v78
	v_pk_add_f32 v[60:61], v[60:61], v[62:63]
	v_lshlrev_b32_e32 v62, 16, v77
	v_and_b32_e32 v63, 0xffff0000, v77
	v_lshlrev_b32_e32 v76, 16, v79
	v_and_b32_e32 v77, 0xffff0000, v79
	v_pk_add_f32 v[78:79], v[80:81], v[82:83]
	v_pk_add_f32 v[6:7], v[6:7], v[8:9]
	v_pk_add_f32 v[8:9], v[66:67], v[84:85]
	v_pk_add_f32 v[52:53], v[52:53], v[54:55]
	v_pk_add_f32 v[54:55], v[70:71], v[88:89]
	v_pk_add_f32 v[60:61], v[60:61], v[62:63]
	v_pk_add_f32 v[62:63], v[78:79], v[96:97]
	v_pk_add_f32 v[8:9], v[8:9], v[86:87]
	v_pk_add_f32 v[56:57], v[56:57], v[58:59]
	v_pk_add_f32 v[58:59], v[74:75], v[92:93]
	v_pk_add_f32 v[54:55], v[54:55], v[90:91]
	s_waitcnt vmcnt(3)
	v_pk_fma_f32 v[16:17], v[36:37], v[62:63], v[16:17]
	s_waitcnt vmcnt(2)
	v_pk_fma_f32 v[20:21], v[40:41], v[8:9], v[20:21]
	v_pk_add_f32 v[6:7], v[6:7], v[64:65]
	v_pk_add_f32 v[52:53], v[52:53], v[68:69]
	v_pk_add_f32 v[58:59], v[58:59], v[94:95]
	s_waitcnt vmcnt(1)
	v_pk_fma_f32 v[24:25], v[44:45], v[54:55], v[24:25]
	v_mul_f32_e32 v8, v17, v17
	v_mul_f32_e32 v9, v21, v21
	v_pk_add_f32 v[56:57], v[56:57], v[72:73]
	v_pk_add_f32 v[60:61], v[60:61], v[76:77]
	v_pk_fma_f32 v[6:7], v[38:39], v[6:7], v[18:19]
	v_pk_fma_f32 v[18:19], v[42:43], v[52:53], v[22:23]
	s_waitcnt vmcnt(0)
	v_pk_fma_f32 v[28:29], v[48:49], v[58:59], v[28:29]
	v_mul_f32_e32 v15, v25, v25
	v_fmac_f32_e32 v8, v16, v16
	v_fmac_f32_e32 v9, v20, v20
	v_pk_fma_f32 v[22:23], v[46:47], v[56:57], v[26:27]
	v_pk_fma_f32 v[26:27], v[50:51], v[60:61], v[30:31]
	v_mul_f32_e32 v30, v29, v29
	v_fmac_f32_e32 v15, v24, v24
	v_fmac_f32_e32 v8, v6, v6
	v_fmac_f32_e32 v9, v18, v18
	v_fmac_f32_e32 v30, v28, v28
	v_fmac_f32_e32 v15, v22, v22
	v_fmac_f32_e32 v8, v7, v7
	v_fmac_f32_e32 v9, v19, v19
	v_fmac_f32_e32 v30, v26, v26
	v_fmac_f32_e32 v15, v23, v23
	v_add_f32_e32 v8, v8, v9
	v_fmac_f32_e32 v30, v27, v27
	v_add_f32_e32 v8, v8, v15
	v_add_f32_e32 v8, v8, v30
	s_nop 1
	v_add_f32_dpp v8, v8, v8 quad_perm:[1,0,3,2] row_mask:0xf bank_mask:0xf bound_ctrl:1
	s_nop 1
	v_add_f32_dpp v8, v8, v8 quad_perm:[2,3,0,1] row_mask:0xf bank_mask:0xf bound_ctrl:1
	s_nop 1
	v_add_f32_dpp v8, v8, v8 row_half_mirror row_mask:0xf bank_mask:0xf bound_ctrl:1
	s_nop 1
	v_add_f32_dpp v8, v8, v8 row_mirror row_mask:0xf bank_mask:0xf bound_ctrl:1
	v_mov_b32_e32 v9, v8
	s_nop 1
	v_permlane16_swap_b32_e32 v8, v9
	v_add_f32_e32 v8, v8, v9
	v_mov_b32_e32 v9, v8
	s_nop 1
	v_permlane32_swap_b32_e32 v8, v9
	v_add_f32_e32 v8, v8, v9
	v_fmamk_f32 v8, v8, 0x3a800000, v14
	v_mul_f32_e32 v9, 0x4b800000, v8
	v_cmp_gt_f32_e32 vcc, s2, v8
	s_nop 1
	v_cndmask_b32_e32 v8, v8, v9, vcc
	v_rsq_f32_e32 v8, v8
	s_nop 0
	v_mul_f32_e32 v9, 0x45800000, v8
	v_cndmask_b32_e32 v30, v8, v9, vcc
	v_pk_mul_f32 v[16:17], v[16:17], v[30:31] op_sel_hi:[1,0]
	v_pk_mul_f32 v[6:7], v[6:7], v[30:31] op_sel_hi:[1,0]
	s_nop 0
	v_pk_mul_f32 v[8:9], v[100:101], v[6:7]
	v_pk_mul_f32 v[6:7], v[98:99], v[16:17]
	global_store_dwordx4 v[4:5], v[6:9], off offset:-3072
	v_pk_mul_f32 v[16:17], v[18:19], v[30:31] op_sel_hi:[1,0]
	v_pk_mul_f32 v[18:19], v[20:21], v[30:31] op_sel_hi:[1,0]
	s_nop 0
	v_pk_mul_f32 v[34:35], v[104:105], v[16:17]
	v_pk_mul_f32 v[32:33], v[102:103], v[18:19]
	global_store_dwordx4 v[4:5], v[32:35], off offset:-2048
	v_pk_mul_f32 v[16:17], v[22:23], v[30:31] op_sel_hi:[1,0]
	v_pk_mul_f32 v[18:19], v[24:25], v[30:31] op_sel_hi:[1,0]
	s_nop 0
	v_pk_mul_f32 v[46:47], v[108:109], v[16:17]
	v_pk_mul_f32 v[44:45], v[106:107], v[18:19]
	global_store_dwordx4 v[4:5], v[44:47], off offset:-1024
	v_pk_mul_f32 v[16:17], v[26:27], v[30:31] op_sel_hi:[1,0]
	v_pk_mul_f32 v[18:19], v[28:29], v[30:31] op_sel_hi:[1,0]
	s_nop 0
	v_pk_mul_f32 v[42:43], v[112:113], v[16:17]
	v_pk_mul_f32 v[40:41], v[110:111], v[18:19]
	global_store_dwordx4 v[4:5], v[40:43], off
	v_lshl_add_u64 v[4:5], v[4:5], 0, s[10:11]
	s_cbranch_scc1 .LBB0_1932
